# topic loop computes w*relu(y) directly: relu via clamp on the add with exact power-of-two pre-scaling (2^-96 on base tile and topic terms, 2^96 on weights); removes linear-term bookkeeping
# speedup vs baseline: 1.0166x; 1.0166x over previous
.LBB1_40:
	s_or_b64 exec, exec, s[8:9]
	s_waitcnt vmcnt(20)
	v_add_f32_e32 v66, 0, v68
	s_waitcnt vmcnt(19)
	v_add_f32_e32 v66, v66, v69
	s_waitcnt vmcnt(18)
	v_add_f32_e32 v66, v66, v70
	s_waitcnt vmcnt(17)
	v_add_f32_e32 v66, v66, v71
	s_waitcnt vmcnt(16)
	v_add_f32_e32 v246, v66, v72
	v_lshlrev_b32_e32 v66, 11, v227
	v_lshl_or_b32 v68, s43, 13, v66
	v_or_b32_e32 v66, v68, v238
	v_or_b32_e32 v77, v68, v0
	v_ashrrev_i32_e32 v67, 31, v66
	v_or_b32_e32 v68, 0x380, v77
	v_lshl_add_u64 v[66:67], v[66:67], 2, s[4:5]
	v_ashrrev_i32_e32 v69, 31, v68
	v_max_f32_e32 v245, 1.0, v73
	s_barrier
	global_load_dword v70, v[66:67], off sc1
	global_load_dword v71, v[66:67], off offset:512 sc1
	global_load_dword v72, v[66:67], off offset:1024 sc1
	global_load_dword v73, v[66:67], off offset:1536 sc1
	global_load_dword v74, v[66:67], off offset:2048 sc1
	global_load_dword v75, v[66:67], off offset:2560 sc1
	global_load_dword v76, v[66:67], off offset:3072 sc1
	v_lshl_add_u64 v[68:69], v[68:69], 2, s[4:5]
	global_load_dword v68, v[68:69], off sc1
	s_movk_i32 s2, 0x1000
	v_add_co_u32_e32 v66, vcc, s2, v66
	v_lshlrev_b32_e32 v211, 2, v214
	s_nop 0
	v_addc_co_u32_e32 v67, vcc, 0, v67, vcc
	global_load_dword v69, v[66:67], off sc1
	global_load_dword v78, v[66:67], off offset:512 sc1
	global_load_dword v79, v[66:67], off offset:1024 sc1
	global_load_dword v80, v[66:67], off offset:1536 sc1
	global_load_dword v81, v[66:67], off offset:2048 sc1
	global_load_dword v214, v[66:67], off offset:2560 sc1
	global_load_dword v215, v[66:67], off offset:3072 sc1
	v_or_b32_e32 v66, 0x780, v77
	v_ashrrev_i32_e32 v67, 31, v66
	s_mov_b32 s2, 0xccccccd
	v_lshl_add_u64 v[66:67], v[66:67], 2, s[4:5]
	v_mul_hi_u32 v244, v0, s2
	global_load_dword v247, v[66:67], off sc1
	v_mul_u32_u24_e32 v66, 20, v244
	s_movk_i32 s2, 0x140
	v_sub_u32_e32 v77, v0, v66
	v_cmp_gt_u32_e64 s[2:3], s2, v0
	v_lshlrev_b32_e32 v66, 3, v244
	v_mov_b32_e32 v67, 0x78
	v_cndmask_b32_e64 v216, v67, v66, s[2:3]
	v_mul_u32_u24_e32 v66, 20, v216
	v_or_b32_e32 v212, v66, v77
	v_mov_b32_e32 v213, 0
	v_lshl_add_u64 v[66:67], v[212:213], 2, s[14:15]
	v_mad_u32_u24 v212, v216, 20, v77
	global_load_dword v220, v[66:67], off
	v_lshl_add_u64 v[66:67], v[212:213], 2, s[14:15]
	global_load_dword v221, v[66:67], off offset:80
	global_load_dword v222, v[66:67], off offset:160
	global_load_dword v223, v[66:67], off offset:240
	global_load_dword v218, v[66:67], off offset:320
	global_load_dword v219, v[66:67], off offset:400
	global_load_dword v216, v[66:67], off offset:480
	global_load_dword v217, v[66:67], off offset:560
	v_lshlrev_b32_e32 v212, 7, v224
	s_movk_i32 s4, 0x180
	s_waitcnt vmcnt(23)
	v_add_f32_e32 v66, 0, v70
	s_waitcnt vmcnt(22)
	v_add_f32_e32 v66, v66, v71
	s_waitcnt vmcnt(21)
	v_add_f32_e32 v66, v66, v72
	s_waitcnt vmcnt(20)
	v_add_f32_e32 v66, v66, v73
	s_waitcnt vmcnt(19)
	v_add_f32_e32 v66, v66, v74
	s_waitcnt vmcnt(18)
	v_add_f32_e32 v66, v66, v75
	s_waitcnt vmcnt(17)
	v_add_f32_e32 v66, v66, v76
	s_waitcnt vmcnt(16)
	v_add_f32_e32 v66, v66, v68
	s_waitcnt vmcnt(15)
	v_add_f32_e32 v66, v66, v69
	s_waitcnt vmcnt(14)
	v_add_f32_e32 v66, v66, v78
	s_waitcnt vmcnt(13)
	v_add_f32_e32 v66, v66, v79
	s_waitcnt vmcnt(12)
	v_add_f32_e32 v66, v66, v80
	s_waitcnt vmcnt(11)
	v_add_f32_e32 v66, v66, v81
	s_waitcnt vmcnt(10)
	v_add_f32_e32 v66, v66, v214
	s_waitcnt vmcnt(9)
	v_add_f32_e32 v248, v66, v215
	v_lshl_add_u64 v[66:67], s[24:25], 0, v[212:213]
	v_lshlrev_b32_e32 v214, 4, v1
	v_mov_b32_e32 v215, v213
	v_lshl_add_u64 v[78:79], v[66:67], 0, v[214:215]
	global_load_dwordx4 v[66:69], v[78:79], off
	global_load_dwordx4 v[70:73], v[78:79], off offset:32
	global_load_dwordx4 v[74:77], v[78:79], off offset:64
	s_nop 0
	global_load_dwordx4 v[78:81], v[78:79], off offset:96
	s_waitcnt vmcnt(12)
	v_add_f32_e32 v215, v248, v247
	v_add_u32_e32 v213, 0x17280, v210
	v_mul_f32_e32 v239, 0x0f800000, v239
	v_mul_f32_e32 v240, 0x0f800000, v240
	v_mul_f32_e32 v241, 0x0f800000, v241
	v_mul_f32_e32 v242, 0x0f800000, v242
	v_mul_f32_e32 v243, 0x0f800000, v243
	ds_write2st64_b32 v210, v239, v240 offset1:8
	ds_write2st64_b32 v210, v242, v241 offset0:16 offset1:24
	ds_write_b32 v210, v243 offset:8192
	ds_write_b32 v213, v215
	v_and_or_b32 v215, v0, s4, v238
	v_mov_b32_e32 v238, 0x17a80
	s_movk_i32 s4, 0x80
	v_lshl_add_u32 v215, v215, 2, v238
	v_cmp_gt_u32_e64 s[4:5], s4, v0
	ds_write_b32 v215, v246
	s_waitcnt lgkmcnt(0)
	s_barrier
	s_and_saveexec_b64 s[6:7], s[4:5]
	s_cbranch_execz .LBB1_42
	v_add_u32_e32 v215, 0x17280, v226
	ds_read2st64_b32 v[238:239], v213 offset0:2 offset1:4
	ds_read_b32 v215, v215
	ds_read2st64_b32 v[240:241], v213 offset0:6 offset1:8
	ds_read2st64_b32 v[242:243], v213 offset0:10 offset1:12
	ds_read_b32 v213, v213 offset:3584
	s_waitcnt lgkmcnt(3)
	v_add_f32_e32 v215, v215, v238
	v_add_f32_e32 v215, v215, v239
	s_waitcnt lgkmcnt(2)
	v_add_f32_e32 v215, v215, v240
	v_div_scale_f32 v238, s[8:9], v245, v245, v215
	v_rcp_f32_e32 v239, v238
	s_waitcnt lgkmcnt(1)
	v_add_f32_e32 v240, v241, v242
	v_add_f32_e32 v240, v240, v243
	s_waitcnt lgkmcnt(0)
	v_add_f32_e32 v213, v240, v213
	v_fma_f32 v240, -v238, v239, 1.0
	v_fmac_f32_e32 v239, v240, v239
	v_div_scale_f32 v240, vcc, v215, v245, v215
	v_mul_f32_e32 v241, v240, v239
	v_fma_f32 v242, -v238, v241, v240
	v_fmac_f32_e32 v241, v242, v239
	v_fma_f32 v238, -v238, v241, v240
	v_div_fmas_f32 v238, v238, v239, v241
	v_div_fixup_f32 v215, v238, v245, v215
	v_add_f32_e32 v215, v237, v215
	v_add_f32_e32 v213, v215, v213
	v_max_f32_e32 v213, 0, v213
	v_add_u32_e32 v215, 0x1b280, v226
	ds_write_b32 v215, v213

.LBB1_53:
	s_or_b64 exec, exec, s[2:3]
	v_add_f32_e32 v130, v130, v14
	v_or_b32_e32 v14, v212, v214
	v_add_f32_e32 v134, v134, v10
	v_add_f32_e32 v10, v110, v50
	v_add_f32_e32 v50, v98, v58
	v_add_f32_e32 v58, v90, v62
	v_add_u32_e32 v62, 0x17080, v14
	v_add_f32_e32 v131, v131, v15
	v_add_f32_e32 v132, v132, v16
	v_add_f32_e32 v133, v133, v17
	v_add_f32_e32 v82, v82, v30
	ds_read_b128 v[14:17], v62
	v_add_f32_e32 v83, v83, v31
	v_add_f32_e32 v84, v84, v32
	v_add_f32_e32 v85, v85, v33
	ds_read_b128 v[30:33], v62 offset:32
	v_add_f32_e32 v2, v142, v2
	v_add_f32_e32 v138, v138, v6
	v_add_f32_e32 v6, v126, v34
	v_add_f32_e32 v34, v122, v38
	v_add_f32_e32 v38, v118, v42
	v_add_f32_e32 v114, v114, v46
	v_add_f32_e32 v42, v106, v54
	v_add_f32_e32 v18, v102, v18
	v_add_f32_e32 v46, v94, v22
	v_add_f32_e32 v141, v141, v9
	v_add_f32_e32 v135, v135, v11
	v_add_f32_e32 v136, v136, v12
	v_add_f32_e32 v137, v137, v13
	v_add_f32_e32 v9, v129, v37
	v_add_f32_e32 v37, v125, v41
	v_add_f32_e32 v41, v121, v45
	v_add_f32_e32 v115, v115, v47
	v_add_f32_e32 v116, v116, v48
	v_add_f32_e32 v117, v117, v49
	v_add_f32_e32 v11, v111, v51
	v_add_f32_e32 v12, v112, v52
	v_add_f32_e32 v13, v113, v53
	v_add_f32_e32 v45, v109, v57
	v_add_f32_e32 v51, v99, v59
	v_add_f32_e32 v52, v100, v60
	v_add_f32_e32 v53, v101, v61
	v_add_f32_e32 v59, v91, v63
	v_add_f32_e32 v60, v92, v64
	v_add_f32_e32 v61, v93, v65
	v_add_f32_e32 v57, v86, v26
	s_waitcnt lgkmcnt(1)
	v_add_f32_e32 v2, v14, v2
	v_add_f32_e32 v6, v14, v6
	v_add_f32_e32 v10, v14, v10
	v_add_f32_e32 v14, v14, v18
	s_waitcnt lgkmcnt(0)
	v_add_f32_e32 v18, v30, v138
	v_add_f32_e32 v22, v30, v34
	v_add_f32_e32 v26, v30, v42
	v_add_f32_e32 v30, v30, v46
	ds_read_b128 v[46:49], v62 offset:64
	ds_read_b128 v[62:65], v62 offset:96
	v_add_f32_e32 v3, v143, v3
	v_add_f32_e32 v4, v144, v4
	v_add_f32_e32 v5, v145, v5
	v_add_f32_e32 v139, v139, v7
	v_add_f32_e32 v140, v140, v8
	v_add_f32_e32 v7, v127, v35
	v_add_f32_e32 v8, v128, v36
	v_add_f32_e32 v35, v123, v39
	v_add_f32_e32 v36, v124, v40
	v_add_f32_e32 v39, v119, v43
	v_add_f32_e32 v40, v120, v44
	v_add_f32_e32 v43, v107, v55
	v_add_f32_e32 v44, v108, v56
	v_add_f32_e32 v19, v103, v19
	v_add_f32_e32 v20, v104, v20
	v_add_f32_e32 v21, v105, v21
	v_add_f32_e32 v54, v95, v23
	v_add_f32_e32 v55, v96, v24
	v_add_f32_e32 v56, v97, v25
	v_add_f32_e32 v86, v87, v27
	v_add_f32_e32 v87, v88, v28
	v_add_f32_e32 v88, v89, v29
	v_add_f32_e32 v3, v15, v3
	v_add_f32_e32 v4, v16, v4
	v_add_f32_e32 v5, v17, v5
	v_add_f32_e32 v7, v15, v7
	v_add_f32_e32 v8, v16, v8
	v_add_f32_e32 v9, v17, v9
	v_add_f32_e32 v11, v15, v11
	v_add_f32_e32 v12, v16, v12
	v_add_f32_e32 v13, v17, v13
	v_add_f32_e32 v15, v15, v19
	v_add_f32_e32 v16, v16, v20
	v_add_f32_e32 v17, v17, v21
	v_add_f32_e32 v19, v31, v139
	v_add_f32_e32 v20, v32, v140
	v_add_f32_e32 v21, v33, v141
	v_add_f32_e32 v23, v31, v35
	v_add_f32_e32 v24, v32, v36
	v_add_f32_e32 v25, v33, v37
	v_add_f32_e32 v27, v31, v43
	v_add_f32_e32 v28, v32, v44
	v_add_f32_e32 v29, v33, v45
	v_add_f32_e32 v31, v31, v54
	v_add_f32_e32 v32, v32, v55
	v_add_f32_e32 v33, v33, v56
	s_waitcnt lgkmcnt(1)
	v_add_f32_e32 v34, v46, v134
	v_add_f32_e32 v38, v46, v38
	v_add_f32_e32 v42, v46, v50
	v_add_f32_e32 v43, v47, v51
	v_add_f32_e32 v44, v48, v52
	v_add_f32_e32 v45, v49, v53
	v_add_f32_e32 v46, v46, v57
	s_waitcnt lgkmcnt(0)
	v_add_f32_e32 v50, v62, v130
	v_add_f32_e32 v51, v63, v131
	v_add_f32_e32 v52, v64, v132
	v_add_f32_e32 v53, v65, v133
	v_add_f32_e32 v54, v62, v114
	v_add_f32_e32 v55, v63, v115
	v_add_f32_e32 v56, v64, v116
	v_add_f32_e32 v57, v65, v117
	v_add_f32_e32 v58, v62, v58
	v_add_f32_e32 v59, v63, v59
	v_add_f32_e32 v60, v64, v60
	v_add_f32_e32 v61, v65, v61
	v_add_f32_e32 v62, v62, v82
	v_add_f32_e32 v63, v63, v83
	v_add_f32_e32 v64, v64, v84
	v_add_f32_e32 v65, v65, v85
	s_waitcnt vmcnt(3)
	s_waitcnt vmcnt(2)
	v_add_f32_e32 v35, v47, v135
	v_add_f32_e32 v39, v47, v39
	v_add_f32_e32 v47, v47, v86
	s_waitcnt vmcnt(1)
	v_add_f32_e32 v36, v48, v136
	v_add_f32_e32 v40, v48, v40
	v_add_f32_e32 v48, v48, v87
	v_add_f32_e32 v37, v49, v137
	v_add_f32_e32 v41, v49, v41
	v_add_f32_e32 v49, v49, v88
	s_waitcnt vmcnt(0)
	v_mul_u32_u24_e32 v87, 10, v225
	v_lshlrev_b32_e32 v1, 9, v1
	v_lshlrev_b32_e32 v86, 9, v87
	v_lshl_or_b32 v1, v87, 12, v1
	v_lshlrev_b32_e32 v87, 10, v224
	v_or3_b32 v1, v87, v1, v211
	v_or3_b32 v86, v86, v212, v214
	v_add_u32_e32 v1, 0x2800, v1
	s_mov_b32 s0, 0
	v_mul_f32_e32 v2, 0x0f800000, v2
	v_mul_f32_e32 v3, 0x0f800000, v3
	v_mul_f32_e32 v4, 0x0f800000, v4
	v_mul_f32_e32 v5, 0x0f800000, v5
	v_mul_f32_e32 v6, 0x0f800000, v6
	v_mul_f32_e32 v7, 0x0f800000, v7
	v_mul_f32_e32 v8, 0x0f800000, v8
	v_mul_f32_e32 v9, 0x0f800000, v9
	v_mul_f32_e32 v10, 0x0f800000, v10
	v_mul_f32_e32 v11, 0x0f800000, v11
	v_mul_f32_e32 v12, 0x0f800000, v12
	v_mul_f32_e32 v13, 0x0f800000, v13
	v_mul_f32_e32 v14, 0x0f800000, v14
	v_mul_f32_e32 v15, 0x0f800000, v15
	v_mul_f32_e32 v16, 0x0f800000, v16
	v_mul_f32_e32 v17, 0x0f800000, v17
	v_mul_f32_e32 v18, 0x0f800000, v18
	v_mul_f32_e32 v19, 0x0f800000, v19
	v_mul_f32_e32 v20, 0x0f800000, v20
	v_mul_f32_e32 v21, 0x0f800000, v21
	v_mul_f32_e32 v22, 0x0f800000, v22
	v_mul_f32_e32 v23, 0x0f800000, v23
	v_mul_f32_e32 v24, 0x0f800000, v24
	v_mul_f32_e32 v25, 0x0f800000, v25
	v_mul_f32_e32 v26, 0x0f800000, v26
	v_mul_f32_e32 v27, 0x0f800000, v27
	v_mul_f32_e32 v28, 0x0f800000, v28
	v_mul_f32_e32 v29, 0x0f800000, v29
	v_mul_f32_e32 v30, 0x0f800000, v30
	v_mul_f32_e32 v31, 0x0f800000, v31
	v_mul_f32_e32 v32, 0x0f800000, v32
	v_mul_f32_e32 v33, 0x0f800000, v33
	v_mul_f32_e32 v34, 0x0f800000, v34
	v_mul_f32_e32 v35, 0x0f800000, v35
	v_mul_f32_e32 v36, 0x0f800000, v36
	v_mul_f32_e32 v37, 0x0f800000, v37
	v_mul_f32_e32 v38, 0x0f800000, v38
	v_mul_f32_e32 v39, 0x0f800000, v39
	v_mul_f32_e32 v40, 0x0f800000, v40
	v_mul_f32_e32 v41, 0x0f800000, v41
	v_mul_f32_e32 v42, 0x0f800000, v42
	v_mul_f32_e32 v43, 0x0f800000, v43
	v_mul_f32_e32 v44, 0x0f800000, v44
	v_mul_f32_e32 v45, 0x0f800000, v45
	v_mul_f32_e32 v46, 0x0f800000, v46
	v_mul_f32_e32 v47, 0x0f800000, v47
	v_mul_f32_e32 v48, 0x0f800000, v48
	v_mul_f32_e32 v49, 0x0f800000, v49
	v_mul_f32_e32 v50, 0x0f800000, v50
	v_mul_f32_e32 v51, 0x0f800000, v51
	v_mul_f32_e32 v52, 0x0f800000, v52
	v_mul_f32_e32 v53, 0x0f800000, v53
	v_mul_f32_e32 v54, 0x0f800000, v54
	v_mul_f32_e32 v55, 0x0f800000, v55
	v_mul_f32_e32 v56, 0x0f800000, v56
	v_mul_f32_e32 v57, 0x0f800000, v57
	v_mul_f32_e32 v58, 0x0f800000, v58
	v_mul_f32_e32 v59, 0x0f800000, v59
	v_mul_f32_e32 v60, 0x0f800000, v60
	v_mul_f32_e32 v61, 0x0f800000, v61
	v_mul_f32_e32 v62, 0x0f800000, v62
	v_mul_f32_e32 v63, 0x0f800000, v63
	v_mul_f32_e32 v64, 0x0f800000, v64
	v_mul_f32_e32 v65, 0x0f800000, v65
	v_mul_f32_e32 v66, 0x6f800000, v66
	v_mul_f32_e32 v67, 0x6f800000, v67
	v_mul_f32_e32 v68, 0x6f800000, v68
	v_mul_f32_e32 v69, 0x6f800000, v69
	v_mul_f32_e32 v70, 0x6f800000, v70
	v_mul_f32_e32 v71, 0x6f800000, v71
	v_mul_f32_e32 v72, 0x6f800000, v72
	v_mul_f32_e32 v73, 0x6f800000, v73
	v_mul_f32_e32 v74, 0x6f800000, v74
	v_mul_f32_e32 v75, 0x6f800000, v75
	v_mul_f32_e32 v76, 0x6f800000, v76
	v_mul_f32_e32 v77, 0x6f800000, v77
	v_mul_f32_e32 v78, 0x6f800000, v78
	v_mul_f32_e32 v79, 0x6f800000, v79
	v_mul_f32_e32 v80, 0x6f800000, v80
	v_mul_f32_e32 v81, 0x6f800000, v81
	v_add_u32_e32 v152, s0, v86
	ds_read_b128 v[88:91], v152
	ds_read_b128 v[92:95], v152 offset:32
	ds_read_b128 v[96:99], v152 offset:64
	ds_read_b128 v[100:103], v152 offset:96
	s_addk_i32 s0, 0x200
.Ltopic_loop:
	v_add_u32_e32 v152, s0, v86
	ds_read_b128 v[136:139], v152
	ds_read_b128 v[140:143], v152 offset:32
	ds_read_b128 v[144:147], v152 offset:64
	ds_read_b128 v[148:151], v152 offset:96
	s_addk_i32 s0, 0x200
	s_waitcnt lgkmcnt(4)
	v_add_f32_e64 v104, v2, v88 clamp
	v_add_f32_e64 v108, v6, v88 clamp
	v_add_f32_e64 v112, v10, v88 clamp
	v_add_f32_e64 v116, v14, v88 clamp
	v_add_f32_e64 v105, v3, v89 clamp
	v_add_f32_e64 v109, v7, v89 clamp
	v_add_f32_e64 v113, v11, v89 clamp
	v_add_f32_e64 v117, v15, v89 clamp
	v_add_f32_e64 v106, v4, v90 clamp
	v_add_f32_e64 v110, v8, v90 clamp
	v_add_f32_e64 v114, v12, v90 clamp
	v_add_f32_e64 v118, v16, v90 clamp
	v_add_f32_e64 v107, v5, v91 clamp
	v_add_f32_e64 v111, v9, v91 clamp
	v_add_f32_e64 v115, v13, v91 clamp
	v_add_f32_e64 v119, v17, v91 clamp
	v_mul_f32_e32 v160, v66, v104
	v_mul_f32_e32 v161, v66, v108
	v_mul_f32_e32 v162, v66, v112
	v_mul_f32_e32 v163, v66, v116
	v_fmac_f32_e32 v160, v67, v105
	v_fmac_f32_e32 v161, v67, v109
	v_fmac_f32_e32 v162, v67, v113
	v_fmac_f32_e32 v163, v67, v117
	v_fmac_f32_e32 v160, v68, v106
	v_fmac_f32_e32 v161, v68, v110
	v_fmac_f32_e32 v162, v68, v114
	v_fmac_f32_e32 v163, v68, v118
	v_fmac_f32_e32 v160, v69, v107
	v_fmac_f32_e32 v161, v69, v111
	v_fmac_f32_e32 v162, v69, v115
	v_fmac_f32_e32 v163, v69, v119
	v_add_f32_e64 v120, v18, v92 clamp
	v_add_f32_e64 v124, v22, v92 clamp
	v_add_f32_e64 v128, v26, v92 clamp
	v_add_f32_e64 v132, v30, v92 clamp
	v_add_f32_e64 v121, v19, v93 clamp
	v_add_f32_e64 v125, v23, v93 clamp
	v_add_f32_e64 v129, v27, v93 clamp
	v_add_f32_e64 v133, v31, v93 clamp
	v_add_f32_e64 v122, v20, v94 clamp
	v_add_f32_e64 v126, v24, v94 clamp
	v_add_f32_e64 v130, v28, v94 clamp
	v_add_f32_e64 v134, v32, v94 clamp
	v_add_f32_e64 v123, v21, v95 clamp
	v_add_f32_e64 v127, v25, v95 clamp
	v_add_f32_e64 v131, v29, v95 clamp
	v_add_f32_e64 v135, v33, v95 clamp
	v_fmac_f32_e32 v160, v70, v120
	v_fmac_f32_e32 v161, v70, v124
	v_fmac_f32_e32 v162, v70, v128
	v_fmac_f32_e32 v163, v70, v132
	v_fmac_f32_e32 v160, v71, v121
	v_fmac_f32_e32 v161, v71, v125
	v_fmac_f32_e32 v162, v71, v129
	v_fmac_f32_e32 v163, v71, v133
	v_fmac_f32_e32 v160, v72, v122
	v_fmac_f32_e32 v161, v72, v126
	v_fmac_f32_e32 v162, v72, v130
	v_fmac_f32_e32 v163, v72, v134
	v_fmac_f32_e32 v160, v73, v123
	v_fmac_f32_e32 v161, v73, v127
	v_fmac_f32_e32 v162, v73, v131
	v_fmac_f32_e32 v163, v73, v135
	v_add_f32_e64 v104, v34, v96 clamp
	v_add_f32_e64 v108, v38, v96 clamp
	v_add_f32_e64 v112, v42, v96 clamp
	v_add_f32_e64 v116, v46, v96 clamp
	v_add_f32_e64 v105, v35, v97 clamp
	v_add_f32_e64 v109, v39, v97 clamp
	v_add_f32_e64 v113, v43, v97 clamp
	v_add_f32_e64 v117, v47, v97 clamp
	v_add_f32_e64 v106, v36, v98 clamp
	v_add_f32_e64 v110, v40, v98 clamp
	v_add_f32_e64 v114, v44, v98 clamp
	v_add_f32_e64 v118, v48, v98 clamp
	v_add_f32_e64 v107, v37, v99 clamp
	v_add_f32_e64 v111, v41, v99 clamp
	v_add_f32_e64 v115, v45, v99 clamp
	v_add_f32_e64 v119, v49, v99 clamp
	v_fmac_f32_e32 v160, v74, v104
	v_fmac_f32_e32 v161, v74, v108
	v_fmac_f32_e32 v162, v74, v112
	v_fmac_f32_e32 v163, v74, v116
	v_fmac_f32_e32 v160, v75, v105
	v_fmac_f32_e32 v161, v75, v109
	v_fmac_f32_e32 v162, v75, v113
	v_fmac_f32_e32 v163, v75, v117
	v_fmac_f32_e32 v160, v76, v106
	v_fmac_f32_e32 v161, v76, v110
	v_fmac_f32_e32 v162, v76, v114
	v_fmac_f32_e32 v163, v76, v118
	v_fmac_f32_e32 v160, v77, v107
	v_fmac_f32_e32 v161, v77, v111
	v_fmac_f32_e32 v162, v77, v115
	v_fmac_f32_e32 v163, v77, v119
	v_add_f32_e64 v120, v50, v100 clamp
	v_add_f32_e64 v124, v54, v100 clamp
	v_add_f32_e64 v128, v58, v100 clamp
	v_add_f32_e64 v132, v62, v100 clamp
	v_add_f32_e64 v121, v51, v101 clamp
	v_add_f32_e64 v125, v55, v101 clamp
	v_add_f32_e64 v129, v59, v101 clamp
	v_add_f32_e64 v133, v63, v101 clamp
	v_add_f32_e64 v122, v52, v102 clamp
	v_add_f32_e64 v126, v56, v102 clamp
	v_add_f32_e64 v130, v60, v102 clamp
	v_add_f32_e64 v134, v64, v102 clamp
	v_add_f32_e64 v123, v53, v103 clamp
	v_add_f32_e64 v127, v57, v103 clamp
	v_add_f32_e64 v131, v61, v103 clamp
	v_add_f32_e64 v135, v65, v103 clamp
	v_fmac_f32_e32 v160, v78, v120
	v_fmac_f32_e32 v161, v78, v124
	v_fmac_f32_e32 v162, v78, v128
	v_fmac_f32_e32 v163, v78, v132
	v_fmac_f32_e32 v160, v79, v121
	v_fmac_f32_e32 v161, v79, v125
	v_fmac_f32_e32 v162, v79, v129
	v_fmac_f32_e32 v163, v79, v133
	v_fmac_f32_e32 v160, v80, v122
	v_fmac_f32_e32 v161, v80, v126
	v_fmac_f32_e32 v162, v80, v130
	v_fmac_f32_e32 v163, v80, v134
	v_fmac_f32_e32 v160, v81, v123
	v_fmac_f32_e32 v161, v81, v127
	v_fmac_f32_e32 v162, v81, v131
	v_fmac_f32_e32 v163, v81, v135
	ds_write2_b32 v1, v160, v161 offset1:32
	ds_write2_b32 v1, v162, v163 offset0:64 offset1:96
	v_add_u32_e32 v1, 0x1000, v1
	v_add_u32_e32 v152, s0, v86
	ds_read_b128 v[88:91], v152
	ds_read_b128 v[92:95], v152 offset:32
	ds_read_b128 v[96:99], v152 offset:64
	ds_read_b128 v[100:103], v152 offset:96
	s_addk_i32 s0, 0x200
	s_waitcnt lgkmcnt(4)
	v_add_f32_e64 v104, v2, v136 clamp
	v_add_f32_e64 v108, v6, v136 clamp
	v_add_f32_e64 v112, v10, v136 clamp
	v_add_f32_e64 v116, v14, v136 clamp
	v_add_f32_e64 v105, v3, v137 clamp
	v_add_f32_e64 v109, v7, v137 clamp
	v_add_f32_e64 v113, v11, v137 clamp
	v_add_f32_e64 v117, v15, v137 clamp
	v_add_f32_e64 v106, v4, v138 clamp
	v_add_f32_e64 v110, v8, v138 clamp
	v_add_f32_e64 v114, v12, v138 clamp
	v_add_f32_e64 v118, v16, v138 clamp
	v_add_f32_e64 v107, v5, v139 clamp
	v_add_f32_e64 v111, v9, v139 clamp
	v_add_f32_e64 v115, v13, v139 clamp
	v_add_f32_e64 v119, v17, v139 clamp
	v_mul_f32_e32 v160, v66, v104
	v_mul_f32_e32 v161, v66, v108
	v_mul_f32_e32 v162, v66, v112
	v_mul_f32_e32 v163, v66, v116
	v_fmac_f32_e32 v160, v67, v105
	v_fmac_f32_e32 v161, v67, v109
	v_fmac_f32_e32 v162, v67, v113
	v_fmac_f32_e32 v163, v67, v117
	v_fmac_f32_e32 v160, v68, v106
	v_fmac_f32_e32 v161, v68, v110
	v_fmac_f32_e32 v162, v68, v114
	v_fmac_f32_e32 v163, v68, v118
	v_fmac_f32_e32 v160, v69, v107
	v_fmac_f32_e32 v161, v69, v111
	v_fmac_f32_e32 v162, v69, v115
	v_fmac_f32_e32 v163, v69, v119
	v_add_f32_e64 v120, v18, v140 clamp
	v_add_f32_e64 v124, v22, v140 clamp
	v_add_f32_e64 v128, v26, v140 clamp
	v_add_f32_e64 v132, v30, v140 clamp
	v_add_f32_e64 v121, v19, v141 clamp
	v_add_f32_e64 v125, v23, v141 clamp
	v_add_f32_e64 v129, v27, v141 clamp
	v_add_f32_e64 v133, v31, v141 clamp
	v_add_f32_e64 v122, v20, v142 clamp
	v_add_f32_e64 v126, v24, v142 clamp
	v_add_f32_e64 v130, v28, v142 clamp
	v_add_f32_e64 v134, v32, v142 clamp
	v_add_f32_e64 v123, v21, v143 clamp
	v_add_f32_e64 v127, v25, v143 clamp
	v_add_f32_e64 v131, v29, v143 clamp
	v_add_f32_e64 v135, v33, v143 clamp
	v_fmac_f32_e32 v160, v70, v120
	v_fmac_f32_e32 v161, v70, v124
	v_fmac_f32_e32 v162, v70, v128
	v_fmac_f32_e32 v163, v70, v132
	v_fmac_f32_e32 v160, v71, v121
	v_fmac_f32_e32 v161, v71, v125
	v_fmac_f32_e32 v162, v71, v129
	v_fmac_f32_e32 v163, v71, v133
	v_fmac_f32_e32 v160, v72, v122
	v_fmac_f32_e32 v161, v72, v126
	v_fmac_f32_e32 v162, v72, v130
	v_fmac_f32_e32 v163, v72, v134
	v_fmac_f32_e32 v160, v73, v123
	v_fmac_f32_e32 v161, v73, v127
	v_fmac_f32_e32 v162, v73, v131
	v_fmac_f32_e32 v163, v73, v135
	v_add_f32_e64 v104, v34, v144 clamp
	v_add_f32_e64 v108, v38, v144 clamp
	v_add_f32_e64 v112, v42, v144 clamp
	v_add_f32_e64 v116, v46, v144 clamp
	v_add_f32_e64 v105, v35, v145 clamp
	v_add_f32_e64 v109, v39, v145 clamp
	v_add_f32_e64 v113, v43, v145 clamp
	v_add_f32_e64 v117, v47, v145 clamp
	v_add_f32_e64 v106, v36, v146 clamp
	v_add_f32_e64 v110, v40, v146 clamp
	v_add_f32_e64 v114, v44, v146 clamp
	v_add_f32_e64 v118, v48, v146 clamp
	v_add_f32_e64 v107, v37, v147 clamp
	v_add_f32_e64 v111, v41, v147 clamp
	v_add_f32_e64 v115, v45, v147 clamp
	v_add_f32_e64 v119, v49, v147 clamp
	v_fmac_f32_e32 v160, v74, v104
	v_fmac_f32_e32 v161, v74, v108
	v_fmac_f32_e32 v162, v74, v112
	v_fmac_f32_e32 v163, v74, v116
	v_fmac_f32_e32 v160, v75, v105
	v_fmac_f32_e32 v161, v75, v109
	v_fmac_f32_e32 v162, v75, v113
	v_fmac_f32_e32 v163, v75, v117
	v_fmac_f32_e32 v160, v76, v106
	v_fmac_f32_e32 v161, v76, v110
	v_fmac_f32_e32 v162, v76, v114
	v_fmac_f32_e32 v163, v76, v118
	v_fmac_f32_e32 v160, v77, v107
	v_fmac_f32_e32 v161, v77, v111
	v_fmac_f32_e32 v162, v77, v115
	v_fmac_f32_e32 v163, v77, v119
	v_add_f32_e64 v120, v50, v148 clamp
	v_add_f32_e64 v124, v54, v148 clamp
	v_add_f32_e64 v128, v58, v148 clamp
	v_add_f32_e64 v132, v62, v148 clamp
	v_add_f32_e64 v121, v51, v149 clamp
	v_add_f32_e64 v125, v55, v149 clamp
	v_add_f32_e64 v129, v59, v149 clamp
	v_add_f32_e64 v133, v63, v149 clamp
	v_add_f32_e64 v122, v52, v150 clamp
	v_add_f32_e64 v126, v56, v150 clamp
	v_add_f32_e64 v130, v60, v150 clamp
	v_add_f32_e64 v134, v64, v150 clamp
	v_add_f32_e64 v123, v53, v151 clamp
	v_add_f32_e64 v127, v57, v151 clamp
	v_add_f32_e64 v131, v61, v151 clamp
	v_add_f32_e64 v135, v65, v151 clamp
	v_fmac_f32_e32 v160, v78, v120
	v_fmac_f32_e32 v161, v78, v124
	v_fmac_f32_e32 v162, v78, v128
	v_fmac_f32_e32 v163, v78, v132
	v_fmac_f32_e32 v160, v79, v121
	v_fmac_f32_e32 v161, v79, v125
	v_fmac_f32_e32 v162, v79, v129
	v_fmac_f32_e32 v163, v79, v133
	v_fmac_f32_e32 v160, v80, v122
	v_fmac_f32_e32 v161, v80, v126
	v_fmac_f32_e32 v162, v80, v130
	v_fmac_f32_e32 v163, v80, v134
	v_fmac_f32_e32 v160, v81, v123
	v_fmac_f32_e32 v161, v81, v127
	v_fmac_f32_e32 v162, v81, v131
	v_fmac_f32_e32 v163, v81, v135
	ds_write2_b32 v1, v160, v161 offset1:32
	ds_write2_b32 v1, v162, v163 offset0:64 offset1:96
	v_add_u32_e32 v1, 0x1000, v1
	s_cmpk_eq_i32 s0, 0x1600
	s_cbranch_scc0 .Ltopic_loop
	v_lshl_or_b32 v1, v227, 12, v226
	s_waitcnt lgkmcnt(0)
	s_barrier
	ds_read2st64_b32 v[2:3], v1 offset0:40 offset1:42
	ds_read2st64_b32 v[4:5], v1 offset0:44 offset1:46
	ds_read2st64_b32 v[6:7], v1 offset0:48 offset1:50
	v_or_b32_e32 v13, 16, v227
	s_waitcnt lgkmcnt(2)
	v_add_f32_e32 v2, s18, v2
	v_add_f32_e32 v8, v2, v3
	ds_read2st64_b32 v[2:3], v1 offset0:52 offset1:54
	s_waitcnt lgkmcnt(2)
	v_add_f32_e32 v4, v8, v4
	v_add_f32_e32 v4, v4, v5
	s_waitcnt lgkmcnt(1)
	v_add_f32_e32 v4, v4, v6
	v_add_f32_e32 v4, v4, v7
	s_waitcnt lgkmcnt(0)
	v_add_f32_e32 v2, v4, v2
	v_add_f32_e32 v2, v2, v3
	v_mul_f32_e32 v2, 0xbfb8aa3b, v2
	v_exp_f32_e32 v2, v2
	s_nop 0
	v_add_f32_e32 v4, 1.0, v2
	v_div_scale_f32 v5, s[0:1], v4, v4, 1.0
	v_rcp_f32_e32 v6, v5
	v_div_scale_f32 v7, vcc, 1.0, v4, 1.0
	ds_read2st64_b32 v[2:3], v1 offset0:104 offset1:106
	v_fma_f32 v8, -v5, v6, 1.0
	v_fmac_f32_e32 v6, v8, v6
	v_mul_f32_e32 v8, v7, v6
	v_fma_f32 v9, -v5, v8, v7
	v_fmac_f32_e32 v8, v9, v6
	v_fma_f32 v5, -v5, v8, v7
	v_div_fmas_f32 v5, v5, v6, v8
	v_div_fixup_f32 v8, v5, v4, 1.0
	ds_read2st64_b32 v[4:5], v1 offset0:108 offset1:110
	ds_read2st64_b32 v[6:7], v1 offset0:112 offset1:114
	s_waitcnt lgkmcnt(2)
	v_add_f32_e32 v2, s18, v2
	v_add_f32_e32 v9, v2, v3
	ds_read2st64_b32 v[2:3], v1 offset0:116 offset1:118
	s_waitcnt lgkmcnt(2)
	v_add_f32_e32 v4, v9, v4
	v_add_f32_e32 v4, v4, v5
	s_waitcnt lgkmcnt(1)
	v_add_f32_e32 v4, v4, v6
	v_add_f32_e32 v4, v4, v7
	s_waitcnt lgkmcnt(0)
	v_add_f32_e32 v2, v4, v2
	v_add_f32_e32 v2, v2, v3
	v_mul_f32_e32 v2, 0xbfb8aa3b, v2
	v_exp_f32_e32 v2, v2
	v_lshlrev_b32_e32 v3, 2, v227
	v_or_b32_e32 v6, 8, v227
	v_mov_b32_e32 v7, 0x17000
	v_add_f32_e32 v10, 1.0, v2
	v_div_scale_f32 v5, s[0:1], v10, v10, 1.0
	v_rcp_f32_e32 v11, v5
	v_or_b32_e32 v4, 0x17000, v3
	v_lshl_or_b32 v12, v6, 2, v7
	v_or_b32_e32 v2, 0x17010, v3
	v_or_b32_e32 v3, 0x17030, v3
	v_lshl_or_b32 v7, v13, 2, v7
	ds_read_b32 v4, v4
	ds_read_b32 v14, v2
	ds_read_b32 v12, v12
	ds_read_b32 v15, v3
	ds_read_b32 v16, v7
	s_waitcnt lgkmcnt(4)
	v_fmaak_f32 v2, v8, v4, 0xbc23d70a
	v_max_f32_e32 v8, 0, v2
	v_fma_f32 v2, -v5, v11, 1.0
	v_fmac_f32_e32 v11, v2, v11
	v_div_scale_f32 v4, vcc, 1.0, v10, 1.0
	v_mul_f32_e32 v17, v4, v11
	v_lshl_or_b32 v18, v6, 12, v226
	ds_read2st64_b32 v[2:3], v18 offset0:40 offset1:42
	v_fma_f32 v6, -v5, v17, v4
	v_fmac_f32_e32 v17, v6, v11
	v_fma_f32 v19, -v5, v17, v4
	ds_read2st64_b32 v[4:5], v18 offset0:44 offset1:46
	ds_read2st64_b32 v[6:7], v18 offset0:48 offset1:50
	s_waitcnt lgkmcnt(2)
	v_add_f32_e32 v2, s18, v2
	v_add_f32_e32 v20, v2, v3
	ds_read2st64_b32 v[2:3], v18 offset0:52 offset1:54
	s_waitcnt lgkmcnt(2)
	v_add_f32_e32 v4, v20, v4
	v_add_f32_e32 v4, v4, v5
	s_waitcnt lgkmcnt(1)
	v_add_f32_e32 v4, v4, v6
	v_add_f32_e32 v4, v4, v7
	s_waitcnt lgkmcnt(0)
	v_add_f32_e32 v2, v4, v2
	v_add_f32_e32 v2, v2, v3
	v_mul_f32_e32 v2, 0xbfb8aa3b, v2
	v_exp_f32_e32 v2, v2
	v_div_fmas_f32 v3, v19, v11, v17
	v_div_fixup_f32 v3, v3, v10, 1.0
	v_mov_b32_e32 v9, 0xbc23d70a
	v_add_f32_e32 v10, 1.0, v2
	v_div_scale_f32 v4, s[0:1], v10, v10, 1.0
	v_rcp_f32_e32 v11, v4
	v_fmaak_f32 v2, v3, v14, 0xbc23d70a
	v_max_f32_e32 v2, 0, v2
	v_add_f32_e32 v8, v8, v2
	v_fma_f32 v2, -v4, v11, 1.0
	v_fmac_f32_e32 v11, v2, v11
	v_div_scale_f32 v5, vcc, 1.0, v10, 1.0
	v_mul_f32_e32 v14, v5, v11
	ds_read2st64_b32 v[2:3], v1 offset0:232 offset1:234
	v_fma_f32 v6, -v4, v14, v5
	v_fmac_f32_e32 v14, v6, v11
	v_fma_f32 v17, -v4, v14, v5
	ds_read2st64_b32 v[4:5], v1 offset0:236 offset1:238
	ds_read2st64_b32 v[6:7], v1 offset0:240 offset1:242
	s_waitcnt lgkmcnt(2)
	v_add_f32_e32 v2, s18, v2
	v_add_f32_e32 v18, v2, v3
	ds_read2st64_b32 v[2:3], v1 offset0:244 offset1:246
	s_waitcnt lgkmcnt(2)
	v_add_f32_e32 v1, v18, v4
	v_add_f32_e32 v1, v1, v5
	s_waitcnt lgkmcnt(1)
	v_add_f32_e32 v1, v1, v6
	v_add_f32_e32 v1, v1, v7
	s_waitcnt lgkmcnt(0)
	v_add_f32_e32 v1, v1, v2
	v_add_f32_e32 v1, v1, v3
	v_mul_f32_e32 v1, 0xbfb8aa3b, v1
	v_exp_f32_e32 v1, v1
	v_div_fmas_f32 v2, v17, v11, v14
	v_div_fixup_f32 v2, v2, v10, 1.0
	v_fmaak_f32 v2, v2, v12, 0xbc23d70a
	v_add_f32_e32 v1, 1.0, v1
	v_div_scale_f32 v4, s[0:1], v1, v1, 1.0
	v_rcp_f32_e32 v10, v4
	v_max_f32_e32 v2, 0, v2
	v_add_f32_e32 v8, v8, v2
	v_div_scale_f32 v5, vcc, 1.0, v1, 1.0
	v_fma_f32 v2, -v4, v10, 1.0
	v_fmac_f32_e32 v10, v2, v10
	v_mul_f32_e32 v11, v5, v10
	v_lshl_or_b32 v12, v13, 12, v226
	ds_read2st64_b32 v[2:3], v12 offset0:40 offset1:42
	v_fma_f32 v6, -v4, v11, v5
	v_fmac_f32_e32 v11, v6, v10
	v_fma_f32 v13, -v4, v11, v5
	ds_read2st64_b32 v[4:5], v12 offset0:44 offset1:46
	ds_read2st64_b32 v[6:7], v12 offset0:48 offset1:50
	s_waitcnt lgkmcnt(2)
	v_add_f32_e32 v2, s18, v2
	v_add_f32_e32 v14, v2, v3
	ds_read2st64_b32 v[2:3], v12 offset0:52 offset1:54
	s_waitcnt lgkmcnt(2)
	v_add_f32_e32 v4, v14, v4
	v_add_f32_e32 v4, v4, v5
	s_waitcnt lgkmcnt(1)
	v_add_f32_e32 v4, v4, v6
	v_add_f32_e32 v4, v4, v7
	s_waitcnt lgkmcnt(0)
	v_add_f32_e32 v2, v4, v2
	v_add_f32_e32 v2, v2, v3
	v_mul_f32_e32 v2, 0xbfb8aa3b, v2
	v_exp_f32_e32 v2, v2
	v_div_fmas_f32 v3, v13, v10, v11
	v_div_fixup_f32 v1, v3, v1, 1.0
	v_fmaak_f32 v1, v1, v15, 0xbc23d70a
	v_add_f32_e32 v2, 1.0, v2
	v_div_scale_f32 v3, s[0:1], v2, v2, 1.0
	v_rcp_f32_e32 v4, v3
	v_max_f32_e32 v1, 0, v1
	v_add_f32_e32 v1, v8, v1
	s_lshl_b32 s0, s42, 5
	v_fma_f32 v5, -v3, v4, 1.0
	v_fmac_f32_e32 v4, v5, v4
	v_div_scale_f32 v5, vcc, 1.0, v2, 1.0
	v_mul_f32_e32 v6, v5, v4
	v_fma_f32 v7, -v3, v6, v5
	v_fmac_f32_e32 v6, v7, v4
	v_fma_f32 v3, -v3, v6, v5
	v_div_fmas_f32 v3, v3, v4, v6
	v_div_fixup_f32 v2, v3, v2, 1.0
	v_fmac_f32_e32 v9, v2, v16
	v_max_f32_e32 v2, 0, v9
	v_add_f32_e32 v2, v1, v2
	v_mov_b32_e32 v1, 0x16800
	v_lshl_or_b32 v1, v0, 2, v1
	v_cmp_gt_u32_e32 vcc, s0, v0
	ds_write_b32 v1, v2
	s_waitcnt lgkmcnt(0)
	s_barrier
	s_and_saveexec_b64 s[0:1], vcc
	s_cbranch_execz .LBB1_57
	ds_read2st64_b32 v[2:3], v1 offset1:2
	ds_read2st64_b32 v[4:5], v1 offset0:4 offset1:6
	v_add_u32_e32 v0, s33, v0
	v_ashrrev_i32_e32 v1, 31, v0
	v_lshl_add_u64 v[6:7], v[0:1], 2, s[10:11]
	s_waitcnt lgkmcnt(1)
	v_add_f32_e32 v1, v2, v3
	s_waitcnt lgkmcnt(0)
	v_add_f32_e32 v1, v1, v4
	v_add_f32_e32 v1, v1, v5
	v_add_u32_e32 v0, 0x7d00, v0
	v_mul_f32_e32 v2, 0x3d4ccccd, v1
	v_ashrrev_i32_e32 v1, 31, v0
	v_lshl_add_u64 v[0:1], v[0:1], 2, s[10:11]
	global_store_dword v[6:7], v2, off
	global_store_dword v[0:1], v2, off
